# same as v26 with the kernel entry aligned to 4 KiB (code placement check)
# speedup vs baseline: 1.0031x; 1.0031x over previous
	.text
	.protected	_Z10hybrid_fwd4Args
	.globl	_Z10hybrid_fwd4Args
	.p2align	12
	.type	_Z10hybrid_fwd4Args,@function
